# speedup vs baseline: 1.0182x; 1.0182x over previous
.LBB5_172:
	s_and_b64 vcc, exec, s[0:1]
	v_mov_b32_e32 v24, 0
	s_waitcnt lgkmcnt(0)
	s_barrier
	s_cbranch_vccnz .LBB5_174
	v_mov_b32_e32 v68, 0x23e90
	ds_read_b64 v[126:127], v68
	v_mov_b32_e32 v68, 0xb000
	v_lshl_or_b32 v136, v128, 4, v68
	v_or_b32_e32 v137, 0x23400, v131
	s_waitcnt vmcnt(0)
	ds_read_b128 v[0:3], v137 offset:1024
	ds_read_b128 v[4:7], v137 offset:1088
	ds_read_b128 v[8:11], v137 offset:1152
	ds_read_b128 v[12:15], v137 offset:1216
	ds_read_b128 v[20:23], v137
	ds_read_b128 v[24:27], v137 offset:64
	ds_read_b128 v[36:39], v136
	ds_read_b128 v[40:43], v136 offset:1024
	ds_read_b128 v[44:47], v136 offset:2048
	ds_read_b128 v[48:51], v136 offset:3072
	s_waitcnt lgkmcnt(10)
	v_pk_add_f32 v[68:69], v[120:121], v[126:127] op_sel_hi:[1,0] neg_lo:[0,1] neg_hi:[0,1]
	v_pk_mul_f32 v[68:69], v[126:127], v[68:69] op_sel:[1,0]
	v_pk_fma_f32 v[84:85], v[70:71], v[68:69], v[102:103]
	v_pk_add_f32 v[68:69], v[122:123], v[126:127] op_sel_hi:[1,0] neg_lo:[0,1] neg_hi:[0,1]
	v_pk_mul_f32 v[68:69], v[126:127], v[68:69] op_sel:[1,0]
	v_pk_fma_f32 v[102:103], v[72:73], v[68:69], v[104:105]
	v_pk_add_f32 v[68:69], v[118:119], v[126:127] op_sel_hi:[1,0] neg_lo:[0,1] neg_hi:[0,1]
	v_pk_mul_f32 v[68:69], v[126:127], v[68:69] op_sel:[1,0]
	v_pk_fma_f32 v[104:105], v[74:75], v[68:69], v[106:107]
	v_pk_add_f32 v[68:69], v[124:125], v[126:127] op_sel_hi:[1,0] neg_lo:[0,1] neg_hi:[0,1]
	v_pk_mul_f32 v[68:69], v[126:127], v[68:69] op_sel:[1,0]
	v_pk_fma_f32 v[106:107], v[76:77], v[68:69], v[108:109]
	v_cvt_pk_bf16_f32 v120, v84, v85
	v_cvt_pk_bf16_f32 v121, v102, v103
	v_cvt_pk_bf16_f32 v122, v104, v105
	v_cvt_pk_bf16_f32 v123, v106, v107
	v_pk_add_f32 v[68:69], v[116:117], v[126:127] op_sel_hi:[1,0] neg_lo:[0,1] neg_hi:[0,1]
	v_pk_mul_f32 v[68:69], v[126:127], v[68:69] op_sel:[1,0]
	v_pk_fma_f32 v[86:87], v[96:97], v[68:69], v[86:87]
	v_pk_add_f32 v[68:69], v[114:115], v[126:127] op_sel_hi:[1,0] neg_lo:[0,1] neg_hi:[0,1]
	v_pk_mul_f32 v[68:69], v[126:127], v[68:69] op_sel:[1,0]
	v_pk_fma_f32 v[88:89], v[152:153], v[68:69], v[88:89]
	v_pk_add_f32 v[68:69], v[110:111], v[126:127] op_sel_hi:[1,0] neg_lo:[0,1] neg_hi:[0,1]
	v_pk_mul_f32 v[68:69], v[126:127], v[68:69] op_sel:[1,0]
	v_pk_fma_f32 v[90:91], v[90:91], v[68:69], v[98:99]
	v_pk_add_f32 v[68:69], v[112:113], v[126:127] op_sel_hi:[1,0] neg_lo:[0,1] neg_hi:[0,1]
	v_pk_mul_f32 v[68:69], v[126:127], v[68:69] op_sel:[1,0]
	v_pk_fma_f32 v[92:93], v[92:93], v[68:69], v[100:101]
	v_cvt_pk_bf16_f32 v16, v86, v87
	v_cvt_pk_bf16_f32 v17, v88, v89
	v_cvt_pk_bf16_f32 v18, v90, v91
	v_cvt_pk_bf16_f32 v19, v92, v93
	ds_read_b128 v[28:31], v137 offset:128
	ds_read_b128 v[32:35], v137 offset:192
	ds_read_b128 v[52:55], v136 offset:32768
	ds_read_b128 v[56:59], v136 offset:40960
	ds_read_b128 v[60:63], v136 offset:49152
	ds_read_b128 v[64:67], v136 offset:57344
	s_waitcnt lgkmcnt(6)
	v_mfma_f32_16x16x32_bf16 v[20:23], v[36:39], v[120:123], v[20:23]
	v_mfma_f32_16x16x32_bf16 v[24:27], v[44:47], v[120:123], v[24:27]
	v_mfma_f32_16x16x32_bf16 v[20:23], v[40:43], v[16:19], v[20:23]
	v_mfma_f32_16x16x32_bf16 v[24:27], v[48:51], v[16:19], v[24:27]
	ds_read_b128 v[36:39], v136 offset:4096
	ds_read_b128 v[40:43], v136 offset:5120
	ds_read_b128 v[44:47], v136 offset:6144
	ds_read_b128 v[48:51], v136 offset:7168
	s_waitcnt lgkmcnt(0)
	v_mfma_f32_16x16x32_bf16 v[28:31], v[36:39], v[120:123], v[28:31]
	v_mfma_f32_16x16x32_bf16 v[32:35], v[44:47], v[120:123], v[32:35]
	v_mfma_f32_16x16x32_bf16 v[28:31], v[40:43], v[16:19], v[28:31]
	v_mfma_f32_16x16x32_bf16 v[32:35], v[48:51], v[16:19], v[32:35]
	ds_read_b128 v[36:39], v136 offset:8192
	ds_read_b128 v[40:43], v136 offset:9216
	ds_read_b128 v[44:47], v136 offset:10240
	ds_read_b128 v[48:51], v136 offset:11264
	v_max_f32_e32 v20, 0, v20
	v_max_f32_e32 v21, 0, v21
	v_max_f32_e32 v22, 0, v22
	v_max_f32_e32 v23, 0, v23
	v_max_f32_e32 v24, 0, v24
	v_max_f32_e32 v25, 0, v25
	v_max_f32_e32 v26, 0, v26
	v_max_f32_e32 v27, 0, v27
	v_cvt_pk_bf16_f32 v132, v20, v21
	v_cvt_pk_bf16_f32 v133, v22, v23
	v_cvt_pk_bf16_f32 v134, v24, v25
	v_cvt_pk_bf16_f32 v135, v26, v27
	ds_read_b128 v[20:23], v137 offset:256
	ds_read_b128 v[24:27], v137 offset:320
	v_mfma_f32_16x16x32_bf16 v[0:3], v[52:55], v[132:135], v[0:3]
	v_mfma_f32_16x16x32_bf16 v[4:7], v[56:59], v[132:135], v[4:7]
	v_mfma_f32_16x16x32_bf16 v[8:11], v[60:63], v[132:135], v[8:11]
	v_mfma_f32_16x16x32_bf16 v[12:15], v[64:67], v[132:135], v[12:15]
	ds_read_b128 v[52:55], v136 offset:33792
	ds_read_b128 v[56:59], v136 offset:41984
	ds_read_b128 v[60:63], v136 offset:50176
	ds_read_b128 v[64:67], v136 offset:58368
	s_waitcnt lgkmcnt(4)
	v_mfma_f32_16x16x32_bf16 v[20:23], v[36:39], v[120:123], v[20:23]
	v_mfma_f32_16x16x32_bf16 v[24:27], v[44:47], v[120:123], v[24:27]
	v_mfma_f32_16x16x32_bf16 v[20:23], v[40:43], v[16:19], v[20:23]
	v_mfma_f32_16x16x32_bf16 v[24:27], v[48:51], v[16:19], v[24:27]
	ds_read_b128 v[36:39], v136 offset:12288
	ds_read_b128 v[40:43], v136 offset:13312
	ds_read_b128 v[44:47], v136 offset:14336
	ds_read_b128 v[48:51], v136 offset:15360
	v_max_f32_e32 v28, 0, v28
	v_max_f32_e32 v29, 0, v29
	v_max_f32_e32 v30, 0, v30
	v_max_f32_e32 v31, 0, v31
	v_max_f32_e32 v32, 0, v32
	v_max_f32_e32 v33, 0, v33
	v_max_f32_e32 v34, 0, v34
	v_max_f32_e32 v35, 0, v35
	v_cvt_pk_bf16_f32 v132, v28, v29
	v_cvt_pk_bf16_f32 v133, v30, v31
	v_cvt_pk_bf16_f32 v134, v32, v33
	v_cvt_pk_bf16_f32 v135, v34, v35
	ds_read_b128 v[28:31], v137 offset:384
	ds_read_b128 v[32:35], v137 offset:448
	s_waitcnt lgkmcnt(6)
	v_mfma_f32_16x16x32_bf16 v[0:3], v[52:55], v[132:135], v[0:3]
	v_mfma_f32_16x16x32_bf16 v[4:7], v[56:59], v[132:135], v[4:7]
	v_mfma_f32_16x16x32_bf16 v[8:11], v[60:63], v[132:135], v[8:11]
	v_mfma_f32_16x16x32_bf16 v[12:15], v[64:67], v[132:135], v[12:15]
	ds_read_b128 v[52:55], v136 offset:34816
	ds_read_b128 v[56:59], v136 offset:43008
	ds_read_b128 v[60:63], v136 offset:51200
	ds_read_b128 v[64:67], v136 offset:59392
	s_waitcnt lgkmcnt(4)
	v_mfma_f32_16x16x32_bf16 v[28:31], v[36:39], v[120:123], v[28:31]
	v_mfma_f32_16x16x32_bf16 v[32:35], v[44:47], v[120:123], v[32:35]
	v_mfma_f32_16x16x32_bf16 v[28:31], v[40:43], v[16:19], v[28:31]
	v_mfma_f32_16x16x32_bf16 v[32:35], v[48:51], v[16:19], v[32:35]
	ds_read_b128 v[36:39], v136 offset:16384
	ds_read_b128 v[40:43], v136 offset:17408
	ds_read_b128 v[44:47], v136 offset:18432
	ds_read_b128 v[48:51], v136 offset:19456
	v_max_f32_e32 v20, 0, v20
	v_max_f32_e32 v21, 0, v21
	v_max_f32_e32 v22, 0, v22
	v_max_f32_e32 v23, 0, v23
	v_max_f32_e32 v24, 0, v24
	v_max_f32_e32 v25, 0, v25
	v_max_f32_e32 v26, 0, v26
	v_max_f32_e32 v27, 0, v27
	v_cvt_pk_bf16_f32 v132, v20, v21
	v_cvt_pk_bf16_f32 v133, v22, v23
	v_cvt_pk_bf16_f32 v134, v24, v25
	v_cvt_pk_bf16_f32 v135, v26, v27
	ds_read_b128 v[20:23], v137 offset:512
	ds_read_b128 v[24:27], v137 offset:576
	s_waitcnt lgkmcnt(6)
	v_mfma_f32_16x16x32_bf16 v[0:3], v[52:55], v[132:135], v[0:3]
	v_mfma_f32_16x16x32_bf16 v[4:7], v[56:59], v[132:135], v[4:7]
	v_mfma_f32_16x16x32_bf16 v[8:11], v[60:63], v[132:135], v[8:11]
	v_mfma_f32_16x16x32_bf16 v[12:15], v[64:67], v[132:135], v[12:15]
	ds_read_b128 v[52:55], v136 offset:35840
	ds_read_b128 v[56:59], v136 offset:44032
	ds_read_b128 v[60:63], v136 offset:52224
	ds_read_b128 v[64:67], v136 offset:60416
	s_waitcnt lgkmcnt(4)
	v_mfma_f32_16x16x32_bf16 v[20:23], v[36:39], v[120:123], v[20:23]
	v_mfma_f32_16x16x32_bf16 v[24:27], v[44:47], v[120:123], v[24:27]
	v_mfma_f32_16x16x32_bf16 v[20:23], v[40:43], v[16:19], v[20:23]
	v_mfma_f32_16x16x32_bf16 v[24:27], v[48:51], v[16:19], v[24:27]
	ds_read_b128 v[36:39], v136 offset:20480
	ds_read_b128 v[40:43], v136 offset:21504
	ds_read_b128 v[44:47], v136 offset:22528
	ds_read_b128 v[48:51], v136 offset:23552
	v_max_f32_e32 v28, 0, v28
	v_max_f32_e32 v29, 0, v29
	v_max_f32_e32 v30, 0, v30
	v_max_f32_e32 v31, 0, v31
	v_max_f32_e32 v32, 0, v32
	v_max_f32_e32 v33, 0, v33
	v_max_f32_e32 v34, 0, v34
	v_max_f32_e32 v35, 0, v35
	v_cvt_pk_bf16_f32 v132, v28, v29
	v_cvt_pk_bf16_f32 v133, v30, v31
	v_cvt_pk_bf16_f32 v134, v32, v33
	v_cvt_pk_bf16_f32 v135, v34, v35
	ds_read_b128 v[28:31], v137 offset:640
	ds_read_b128 v[32:35], v137 offset:704
	s_waitcnt lgkmcnt(6)
	v_mfma_f32_16x16x32_bf16 v[0:3], v[52:55], v[132:135], v[0:3]
	v_mfma_f32_16x16x32_bf16 v[4:7], v[56:59], v[132:135], v[4:7]
	v_mfma_f32_16x16x32_bf16 v[8:11], v[60:63], v[132:135], v[8:11]
	v_mfma_f32_16x16x32_bf16 v[12:15], v[64:67], v[132:135], v[12:15]
	ds_read_b128 v[52:55], v136 offset:36864
	ds_read_b128 v[56:59], v136 offset:45056
	ds_read_b128 v[60:63], v136 offset:53248
	ds_read_b128 v[64:67], v136 offset:61440
	s_waitcnt lgkmcnt(4)
	v_mfma_f32_16x16x32_bf16 v[28:31], v[36:39], v[120:123], v[28:31]
	v_mfma_f32_16x16x32_bf16 v[32:35], v[44:47], v[120:123], v[32:35]
	v_mfma_f32_16x16x32_bf16 v[28:31], v[40:43], v[16:19], v[28:31]
	v_mfma_f32_16x16x32_bf16 v[32:35], v[48:51], v[16:19], v[32:35]
	ds_read_b128 v[36:39], v136 offset:24576
	ds_read_b128 v[40:43], v136 offset:25600
	ds_read_b128 v[44:47], v136 offset:26624
	ds_read_b128 v[48:51], v136 offset:27648
	v_max_f32_e32 v20, 0, v20
	v_max_f32_e32 v21, 0, v21
	v_max_f32_e32 v22, 0, v22
	v_max_f32_e32 v23, 0, v23
	v_max_f32_e32 v24, 0, v24
	v_max_f32_e32 v25, 0, v25
	v_max_f32_e32 v26, 0, v26
	v_max_f32_e32 v27, 0, v27
	v_cvt_pk_bf16_f32 v132, v20, v21
	v_cvt_pk_bf16_f32 v133, v22, v23
	v_cvt_pk_bf16_f32 v134, v24, v25
	v_cvt_pk_bf16_f32 v135, v26, v27
	ds_read_b128 v[20:23], v137 offset:768
	ds_read_b128 v[24:27], v137 offset:832
	s_waitcnt lgkmcnt(6)
	v_mfma_f32_16x16x32_bf16 v[0:3], v[52:55], v[132:135], v[0:3]
	v_mfma_f32_16x16x32_bf16 v[4:7], v[56:59], v[132:135], v[4:7]
	v_mfma_f32_16x16x32_bf16 v[8:11], v[60:63], v[132:135], v[8:11]
	v_mfma_f32_16x16x32_bf16 v[12:15], v[64:67], v[132:135], v[12:15]
	ds_read_b128 v[52:55], v136 offset:37888
	ds_read_b128 v[56:59], v136 offset:46080
	ds_read_b128 v[60:63], v136 offset:54272
	ds_read_b128 v[64:67], v136 offset:62464
	s_waitcnt lgkmcnt(4)
	v_mfma_f32_16x16x32_bf16 v[20:23], v[36:39], v[120:123], v[20:23]
	v_mfma_f32_16x16x32_bf16 v[24:27], v[44:47], v[120:123], v[24:27]
	v_mfma_f32_16x16x32_bf16 v[20:23], v[40:43], v[16:19], v[20:23]
	v_mfma_f32_16x16x32_bf16 v[24:27], v[48:51], v[16:19], v[24:27]
	ds_read_b128 v[36:39], v136 offset:28672
	ds_read_b128 v[40:43], v136 offset:29696
	ds_read_b128 v[44:47], v136 offset:30720
	ds_read_b128 v[48:51], v136 offset:31744
	v_max_f32_e32 v28, 0, v28
	v_max_f32_e32 v29, 0, v29
	v_max_f32_e32 v30, 0, v30
	v_max_f32_e32 v31, 0, v31
	v_max_f32_e32 v32, 0, v32
	v_max_f32_e32 v33, 0, v33
	v_max_f32_e32 v34, 0, v34
	v_max_f32_e32 v35, 0, v35
	v_cvt_pk_bf16_f32 v132, v28, v29
	v_cvt_pk_bf16_f32 v133, v30, v31
	v_cvt_pk_bf16_f32 v134, v32, v33
	v_cvt_pk_bf16_f32 v135, v34, v35
	ds_read_b128 v[28:31], v137 offset:896
	ds_read_b128 v[32:35], v137 offset:960
	s_waitcnt lgkmcnt(6)
	v_mfma_f32_16x16x32_bf16 v[0:3], v[52:55], v[132:135], v[0:3]
	v_mfma_f32_16x16x32_bf16 v[4:7], v[56:59], v[132:135], v[4:7]
	v_mfma_f32_16x16x32_bf16 v[8:11], v[60:63], v[132:135], v[8:11]
	v_mfma_f32_16x16x32_bf16 v[12:15], v[64:67], v[132:135], v[12:15]
	ds_read_b128 v[52:55], v136 offset:38912
	ds_read_b128 v[56:59], v136 offset:47104
	ds_read_b128 v[60:63], v136 offset:55296
	ds_read_b128 v[64:67], v136 offset:63488
	s_waitcnt lgkmcnt(4)
	v_mfma_f32_16x16x32_bf16 v[28:31], v[36:39], v[120:123], v[28:31]
	v_mfma_f32_16x16x32_bf16 v[32:35], v[44:47], v[120:123], v[32:35]
	v_mfma_f32_16x16x32_bf16 v[28:31], v[40:43], v[16:19], v[28:31]
	v_mfma_f32_16x16x32_bf16 v[32:35], v[48:51], v[16:19], v[32:35]
	s_nop 3
	v_max_f32_e32 v20, 0, v20
	v_max_f32_e32 v21, 0, v21
	v_max_f32_e32 v22, 0, v22
	v_max_f32_e32 v23, 0, v23
	v_max_f32_e32 v24, 0, v24
	v_max_f32_e32 v25, 0, v25
	v_max_f32_e32 v26, 0, v26
	v_max_f32_e32 v27, 0, v27
	v_cvt_pk_bf16_f32 v132, v20, v21
	v_cvt_pk_bf16_f32 v133, v22, v23
	v_cvt_pk_bf16_f32 v134, v24, v25
	v_cvt_pk_bf16_f32 v135, v26, v27
	s_nop 1
	s_waitcnt lgkmcnt(0)
	v_mfma_f32_16x16x32_bf16 v[0:3], v[52:55], v[132:135], v[0:3]
	v_mfma_f32_16x16x32_bf16 v[4:7], v[56:59], v[132:135], v[4:7]
	v_mfma_f32_16x16x32_bf16 v[8:11], v[60:63], v[132:135], v[8:11]
	v_mfma_f32_16x16x32_bf16 v[12:15], v[64:67], v[132:135], v[12:15]
	ds_read_b128 v[52:55], v136 offset:39936
	ds_read_b128 v[56:59], v136 offset:48128
	ds_read_b128 v[60:63], v136 offset:56320
	ds_read_b128 v[64:67], v136 offset:64512
	s_nop 7
	v_max_f32_e32 v28, 0, v28
	v_max_f32_e32 v29, 0, v29
	v_max_f32_e32 v30, 0, v30
	v_max_f32_e32 v31, 0, v31
	v_max_f32_e32 v32, 0, v32
	v_max_f32_e32 v33, 0, v33
	v_max_f32_e32 v34, 0, v34
	v_max_f32_e32 v35, 0, v35
	v_cvt_pk_bf16_f32 v132, v28, v29
	v_cvt_pk_bf16_f32 v133, v30, v31
	v_cvt_pk_bf16_f32 v134, v32, v33
	v_cvt_pk_bf16_f32 v135, v34, v35
	s_nop 1
	s_waitcnt lgkmcnt(0)
	v_mfma_f32_16x16x32_bf16 v[0:3], v[52:55], v[132:135], v[0:3]
	v_mfma_f32_16x16x32_bf16 v[4:7], v[56:59], v[132:135], v[4:7]
	v_mfma_f32_16x16x32_bf16 v[8:11], v[60:63], v[132:135], v[8:11]
	v_mfma_f32_16x16x32_bf16 v[12:15], v[64:67], v[132:135], v[12:15]
	s_nop 4
	v_pk_add_f32 v[120:121], v[0:1], v[84:85]
	v_pk_add_f32 v[122:123], v[2:3], v[102:103]
	v_pk_add_f32 v[118:119], v[4:5], v[104:105]
	v_pk_add_f32 v[124:125], v[6:7], v[106:107]
	v_pk_add_f32 v[116:117], v[8:9], v[86:87]
	v_pk_add_f32 v[114:115], v[10:11], v[88:89]
	v_pk_add_f32 v[110:111], v[12:13], v[90:91]
	v_pk_add_f32 v[112:113], v[14:15], v[92:93]
	v_mul_f32_e32 v37, v130, v120
	v_mul_f32_e32 v36, v120, v37
	v_pk_add_f32 v[24:25], v[36:37], 0 op_sel_hi:[1,0]
	v_mul_f32_e32 v37, v130, v121
	v_mul_f32_e32 v36, v121, v37
	v_pk_add_f32 v[24:25], v[24:25], v[36:37]
	v_mul_f32_e32 v37, v130, v122
	v_mul_f32_e32 v36, v122, v37
	v_pk_add_f32 v[24:25], v[24:25], v[36:37]
	v_mul_f32_e32 v37, v130, v123
	v_mul_f32_e32 v36, v123, v37
	v_pk_add_f32 v[24:25], v[24:25], v[36:37]
	v_mul_f32_e32 v37, v130, v118
	v_mul_f32_e32 v36, v118, v37
	v_pk_add_f32 v[24:25], v[24:25], v[36:37]
	v_mul_f32_e32 v37, v130, v119
	v_mul_f32_e32 v36, v119, v37
	v_pk_add_f32 v[24:25], v[24:25], v[36:37]
	v_mul_f32_e32 v37, v130, v124
	v_mul_f32_e32 v36, v124, v37
	v_pk_add_f32 v[24:25], v[24:25], v[36:37]
	v_mul_f32_e32 v37, v130, v125
	v_mul_f32_e32 v36, v125, v37
	v_pk_add_f32 v[24:25], v[24:25], v[36:37]
	v_mul_f32_e32 v37, v130, v116
	v_mul_f32_e32 v36, v116, v37
	v_pk_add_f32 v[24:25], v[24:25], v[36:37]
	v_mul_f32_e32 v37, v130, v117
	v_mul_f32_e32 v36, v117, v37
	v_pk_add_f32 v[24:25], v[24:25], v[36:37]
	v_mul_f32_e32 v37, v130, v114
	v_mul_f32_e32 v36, v114, v37
	v_pk_add_f32 v[24:25], v[24:25], v[36:37]
	v_mul_f32_e32 v37, v130, v115
	v_mul_f32_e32 v36, v115, v37
	v_pk_add_f32 v[24:25], v[24:25], v[36:37]
	v_mul_f32_e32 v37, v130, v110
	v_mul_f32_e32 v36, v110, v37
	v_pk_add_f32 v[24:25], v[24:25], v[36:37]
	v_mul_f32_e32 v37, v130, v111
	v_mul_f32_e32 v36, v111, v37
	v_pk_add_f32 v[24:25], v[24:25], v[36:37]
	v_mul_f32_e32 v37, v130, v112
	v_mul_f32_e32 v36, v112, v37
	v_pk_add_f32 v[24:25], v[24:25], v[36:37]
	v_mul_f32_e32 v37, v130, v113
	v_mul_f32_e32 v36, v113, v37
	v_pk_add_f32 v[24:25], v[24:25], v[36:37]
	s_branch .LBB5_175
